# L1 prologue: kernarg loads hoisted, perm/node index loads issued with the tile-info load (on top of wide stores)
# speedup vs baseline: 1.0537x; 1.0023x over previous
.LBB2_2:
	s_andn2_b64 vcc, exec, s[4:5]
	s_cbranch_vccnz .LBB2_14
	s_ashr_i32 s16, s2, 3
	s_lshr_b32 s3, s16, 30
	s_add_i32 s3, s16, s3
	s_load_dwordx2 s[4:5], s[0:1], 0x18
	s_load_dwordx2 s[18:19], s[0:1], 0x10
	s_load_dwordx4 s[8:11], s[0:1], 0x20
	s_load_dwordx2 s[12:13], s[0:1], 0x30
	s_ashr_i32 s17, s3, 2
	s_lshl_b32 s3, s17, 3
	s_and_b32 s2, s2, 7
	s_or_b32 s2, s3, s2
	s_ashr_i32 s3, s2, 31
	s_lshl_b64 s[6:7], s[2:3], 2
	v_readfirstlane_b32 s35, v0
	v_bfe_u32 v3, v0, 3, 3
	s_nop 2
	s_lshr_b32 s21, s35, 6
	v_lshl_or_b32 v5, s21, 4, v3
	v_lshlrev_b32_e32 v1, 2, v5
	s_lshl_b32 s36, s2, 7
	s_ashr_i32 s37, s36, 31
	s_lshl_b64 s[36:37], s[36:37], 2
	s_waitcnt lgkmcnt(0)
	s_add_u32 s4, s4, s6
	s_addc_u32 s5, s5, s7
	s_load_dword s15, s[4:5], 0x0
	s_add_u32 s36, s18, s36
	s_addc_u32 s37, s19, s37
	global_load_dword v2, v1, s[36:37]
	global_load_dword v4, v1, s[36:37] offset:32
	v_and_b32_e32 v1, 15, v0
	s_lshr_b32 s23, s35, 8
	v_lshl_or_b32 v83, s23, 6, v1
	v_lshlrev_b32_e32 v10, 2, v83
	global_load_dword v88, v10, s[36:37]
	global_load_dword v86, v10, s[36:37] offset:64
	global_load_dword v84, v10, s[36:37] offset:128
	global_load_dword v82, v10, s[36:37] offset:192
	s_mov_b32 s14, 0
	s_waitcnt lgkmcnt(0)
	s_cmp_lt_i32 s15, 0
	s_cbranch_scc1 .LBB2_14
	s_lshl_b32 s2, s2, 7
	s_ashr_i32 s3, s2, 31
	s_lshl_b64 s[2:3], s[2:3], 2
	s_add_u32 s2, s18, s2
	s_load_dwordx4 s[4:7], s[0:1], 0x0
	s_addc_u32 s3, s19, s3
	s_lshl_b32 s0, s17, 2
	s_and_b32 s18, s15, 0xff
	s_sub_i32 s0, s16, s0
	s_lshl_b32 s1, s18, 21
	s_add_u32 s19, s8, s1
	v_readfirstlane_b32 s1, v0
	s_addc_u32 s20, s9, 0
	s_lshr_b32 s21, s1, 6
	v_bfe_u32 v3, v0, 3, 3
	v_lshl_or_b32 v5, s21, 4, v3
	v_lshlrev_b32_e32 v1, 2, v5
	s_bfe_u32 s22, s1, 0x20006
	s_lshl_b32 s8, s18, 12
	s_add_u32 s12, s12, s8
	s_addc_u32 s13, s13, 0
	s_lshl_b32 s0, s0, 8
	v_and_b32_e32 v1, 15, v0
	s_lshr_b32 s23, s1, 8
	s_ashr_i32 s1, s0, 31
	v_lshl_or_b32 v83, s23, 6, v1
	s_lshl_b64 s[8:9], s[0:1], 2
	v_lshlrev_b32_e32 v10, 2, v83
	s_add_u32 s12, s12, s8
	s_addc_u32 s2, s13, s9
	s_lshl_b32 s8, s22, 6
	s_lshl_b32 s3, s22, 8
	v_lshrrev_b32_e32 v44, 1, v5
	s_add_u32 s16, s12, s3
	v_lshl_or_b32 v13, s21, 5, v3
	v_or_b32_e32 v3, 8, v5
	v_xor_b32_e32 v7, v44, v0
	s_addc_u32 s17, s2, 0
	s_lshl_b32 s9, s21, 11
	s_lshl_b32 s12, s21, 12
	v_or_b32_e32 v5, 8, v13
	v_lshrrev_b32_e32 v45, 1, v3
	v_lshlrev_b32_e32 v3, 4, v7
	s_add_i32 s13, s9, 0
	s_add_i32 s2, s12, 0
	v_lshrrev_b32_e32 v46, 1, v5
	v_add_u32_e32 v8, s0, v5
	v_xor_b32_e32 v5, v45, v0
	v_and_b32_e32 v18, 0x70, v3
	s_add_i32 s21, s13, 0x400
	s_add_i32 s24, s2, 0x4000
	s_add_i32 s25, s2, 0x4400
	s_add_i32 s26, s2, 0x4800
	s_add_i32 s27, s2, 0x4c00
	s_add_i32 s28, s13, 0xc000
	s_add_i32 s29, s13, 0xc400
	s_add_i32 s30, s2, 0x10000
	s_add_i32 s31, s2, 0x10400
	s_add_i32 s33, s2, 0x10800
	s_add_i32 s34, s2, 0x10c00
	v_lshlrev_b32_e32 v15, 4, v5
	s_cmp_eq_u32 s18, 2
	v_mov_b32_e32 v19, 0
	v_ashrrev_i32_e32 v9, 31, v8
	s_cselect_b32 s2, s10, s19
	s_cselect_b32 s10, 11, 10
	v_bfe_u32 v89, v0, 4, 2
	v_xor_b32_e32 v14, v46, v0
	v_lshlrev_b64 v[8:9], s10, v[8:9]
	v_xor_b32_e32 v6, v89, v0
	s_cselect_b32 s3, s11, s20
	v_lshlrev_b64 v[22:23], 1, v[8:9]
	v_lshlrev_b32_e32 v12, 4, v6
	v_add_u32_e32 v6, s0, v13
	v_ashrrev_i32_e32 v7, 31, v6
	v_lshlrev_b64 v[10:11], s10, v[6:7]
	v_lshlrev_b64 v[20:21], 1, v[10:11]
	v_lshl_add_u64 v[8:9], s[2:3], 0, v[20:21]
	s_mov_b32 m0, s13
	v_mov_b32_e32 v50, v19
	v_mov_b32_e32 v51, v19
	v_mov_b32_e32 v52, v19
	v_mov_b32_e32 v53, v19
	v_mov_b32_e32 v48, v19
	v_mov_b32_e32 v49, v19
	v_mov_b32_e32 v54, v19
	v_mov_b32_e32 v55, v19
	v_mov_b32_e32 v56, v19
	v_mov_b32_e32 v57, v19
	v_mov_b32_e32 v58, v19
	v_mov_b32_e32 v59, v19
	v_mov_b32_e32 v60, v19
	v_mov_b32_e32 v61, v19
	v_mov_b32_e32 v62, v19
	s_waitcnt vmcnt(5)
	v_ashrrev_i32_e32 v3, 31, v2
	s_waitcnt vmcnt(4)
	v_ashrrev_i32_e32 v5, 31, v4
	v_lshlrev_b64 v[24:25], 12, v[2:3]
	v_lshlrev_b64 v[26:27], 12, v[4:5]
	s_waitcnt lgkmcnt(0)
	v_lshl_add_u64 v[2:3], s[4:5], 0, v[24:25]
	v_lshl_add_u64 v[4:5], s[4:5], 0, v[26:27]
	v_lshl_add_u64 v[28:29], v[2:3], 0, v[18:19]
	v_and_b32_e32 v18, 0x70, v15
	v_lshl_add_u64 v[30:31], v[4:5], 0, v[18:19]
	v_lshlrev_b32_e32 v4, 4, v14
	v_lshl_add_u64 v[2:3], s[2:3], 0, v[22:23]
	v_and_b32_e32 v4, 0x70, v4
	v_mov_b32_e32 v5, v19
	v_lshl_add_u64 v[34:35], v[2:3], 0, v[4:5]
	v_or_b32_e32 v2, 16, v6
	v_ashrrev_i32_e32 v3, 31, v2
	v_lshlrev_b64 v[2:3], s10, v[2:3]
	v_lshlrev_b64 v[36:37], 1, v[2:3]
	v_and_b32_e32 v18, 0x70, v12
	v_lshl_add_u64 v[2:3], s[2:3], 0, v[36:37]
	v_lshl_add_u64 v[38:39], v[2:3], 0, v[18:19]
	v_or_b32_e32 v2, 24, v13
	v_lshrrev_b32_e32 v47, 1, v2
	v_add_u32_e32 v2, s0, v2
	v_ashrrev_i32_e32 v3, 31, v2
	v_xor_b32_e32 v4, v47, v0
	v_lshlrev_b64 v[2:3], s10, v[2:3]
	v_lshlrev_b64 v[40:41], 1, v[2:3]
	v_lshlrev_b32_e32 v4, 4, v4
	v_lshl_add_u64 v[32:33], v[8:9], 0, v[18:19]
	v_lshl_add_u64 v[2:3], s[2:3], 0, v[40:41]
	v_and_b32_e32 v18, 0x70, v4
	v_lshl_add_u64 v[42:43], v[2:3], 0, v[18:19]
	v_and_b32_e32 v18, 48, v0
	global_load_dwordx4 v[14:17], v18, s[16:17]
	global_load_dwordx4 v[10:13], v18, s[16:17] offset:64
	global_load_dwordx4 v[6:9], v18, s[16:17] offset:128
	global_load_dwordx4 v[2:5], v18, s[16:17] offset:192
	s_nop 0
	global_load_lds_dwordx4 v[28:29], off
	s_mov_b32 m0, s21
	s_mov_b64 s[10:11], 0x80
	global_load_lds_dwordx4 v[30:31], off
	s_mov_b32 m0, s24
	v_lshl_add_u64 v[28:29], v[28:29], 0, s[10:11]
	global_load_lds_dwordx4 v[32:33], off
	s_mov_b32 m0, s25
	v_bfe_u32 v18, v0, 1, 3
	global_load_lds_dwordx4 v[34:35], off
	s_mov_b32 m0, s26
	s_mov_b64 s[16:17], 0x100
	global_load_lds_dwordx4 v[38:39], off
	s_mov_b32 m0, s27
	v_mov_b32_e32 v63, v19
	global_load_lds_dwordx4 v[42:43], off
	s_mov_b32 m0, s28
	v_mov_b32_e32 v64, v19
	global_load_lds_dwordx4 v[28:29], off
	v_lshl_add_u64 v[28:29], v[30:31], 0, s[10:11]
	s_mov_b32 m0, s29
	v_mov_b32_e32 v30, v19
	global_load_lds_dwordx4 v[28:29], off
	v_lshl_add_u64 v[28:29], v[32:33], 0, s[10:11]
	s_mov_b32 m0, s30
	v_mov_b32_e32 v31, v19
	global_load_lds_dwordx4 v[28:29], off
	v_lshl_add_u64 v[28:29], v[34:35], 0, s[10:11]
	s_mov_b32 m0, s31
	v_mov_b32_e32 v32, v19
	global_load_lds_dwordx4 v[28:29], off
	v_lshl_add_u64 v[28:29], v[38:39], 0, s[10:11]
	s_mov_b32 m0, s33
	v_mov_b32_e32 v33, v19
	global_load_lds_dwordx4 v[28:29], off
	v_lshl_add_u64 v[28:29], v[42:43], 0, s[10:11]
	s_mov_b32 m0, s34
	s_movk_i32 s10, 0xf00
	global_load_lds_dwordx4 v[28:29], off
	v_xor_b32_e32 v28, v89, v18
	v_bitop3_b32 v18, v89, v18, 4 bitop3:0x36
	v_lshlrev_b32_e32 v85, 4, v18
	v_bitop3_b32 v18, v47, 7, v0 bitop3:0x48
	v_lshl_or_b32 v40, v18, 4, v40
	v_bitop3_b32 v18, v89, 7, v0 bitop3:0x48
	v_lshlrev_b32_e32 v18, 4, v18
	v_lshlrev_b32_e32 v87, 4, v28
	v_lshl_add_u64 v[28:29], s[2:3], 0, v[40:41]
	v_or_b32_e32 v36, v36, v18
	v_lshl_add_u64 v[90:91], v[28:29], 0, s[16:17]
	v_lshl_add_u64 v[28:29], s[2:3], 0, v[36:37]
	v_or_b32_e32 v20, v20, v18
	v_bitop3_b32 v18, v45, 7, v0 bitop3:0x48
	v_lshl_add_u64 v[92:93], v[28:29], 0, s[16:17]
	v_bitop3_b32 v28, v46, 7, v0 bitop3:0x48
	v_lshl_add_u64 v[20:21], s[2:3], 0, v[20:21]
	v_lshl_or_b32 v26, v18, 4, v26
	v_bitop3_b32 v0, v44, 7, v0 bitop3:0x48
	v_lshl_or_b32 v22, v28, 4, v22
	v_lshl_add_u64 v[96:97], v[20:21], 0, s[16:17]
	v_lshl_add_u64 v[20:21], s[4:5], 0, v[26:27]
	v_lshl_or_b32 v24, v0, 4, v24
	v_lshl_add_u64 v[22:23], s[2:3], 0, v[22:23]
	v_lshl_add_u64 v[98:99], v[20:21], 0, s[16:17]
	v_lshl_add_u64 v[20:21], s[4:5], 0, v[24:25]
	s_cselect_b32 s10, s10, 0x700
	s_lshl_b32 s11, s23, 13
	s_lshl_b32 s13, s22, 13
	v_lshl_add_u64 v[94:95], v[22:23], 0, s[16:17]
	v_lshl_add_u64 v[100:101], v[20:21], 0, s[16:17]
	s_mov_b64 s[2:3], 0
	v_mov_b32_e32 v18, v19
	v_mov_b32_e32 v20, v19
	v_mov_b32_e32 v21, v19
	v_mov_b32_e32 v22, v19
	v_mov_b32_e32 v23, v19
	v_mov_b32_e32 v24, v19
	v_mov_b32_e32 v25, v19
	v_mov_b32_e32 v26, v19
	v_mov_b32_e32 v27, v19
	v_mov_b32_e32 v28, v19
	v_mov_b32_e32 v29, v19
	v_mov_b32_e32 v38, v19
	v_mov_b32_e32 v39, v19
	v_mov_b32_e32 v40, v19
	v_mov_b32_e32 v41, v19
	v_mov_b32_e32 v42, v19
	v_mov_b32_e32 v43, v19
	v_mov_b32_e32 v44, v19
	v_mov_b32_e32 v45, v19
	v_mov_b32_e32 v46, v19
	v_mov_b32_e32 v47, v19
	v_mov_b32_e32 v65, v19
	v_mov_b32_e32 v66, v19
	v_mov_b32_e32 v67, v19
	v_mov_b32_e32 v68, v19
	v_mov_b32_e32 v69, v19
	v_mov_b32_e32 v70, v19
	v_mov_b32_e32 v71, v19
	v_mov_b32_e32 v72, v19
	v_mov_b32_e32 v73, v19
	v_mov_b32_e32 v74, v19
	v_mov_b32_e32 v75, v19
	v_mov_b32_e32 v76, v19
	v_mov_b32_e32 v77, v19
	v_mov_b32_e32 v34, v19
	v_mov_b32_e32 v35, v19
	v_mov_b32_e32 v36, v19
	v_mov_b32_e32 v37, v19
	v_mov_b32_e32 v78, v19
	v_mov_b32_e32 v79, v19
	v_mov_b32_e32 v80, v19
	v_mov_b32_e32 v81, v19
	v_lshlrev_b32_e32 v0, 2, v89
	v_lshlrev_b32_e32 v89, 7, v1
